# MLA attention softmax: in-place half swaps (v_pk_mov) removed, bf16 pack reads the halves directly
# speedup vs baseline: 1.0010x; 1.0010x over previous
.LBB0_829:
	v_mul_f32_e32 v151, 0x3e16c740, v2
	v_fma_f32 v36, v36, s3, -v151
	v_exp_f32_e32 v154, v36
	v_fma_f32 v36, v53, s3, -v151
	v_fma_f32 v52, v52, s3, -v151
	v_exp_f32_e32 v155, v36
	v_fma_f32 v36, v37, s3, -v151
	v_exp_f32_e32 v153, v52
	v_exp_f32_e32 v156, v36
	v_fma_f32 v36, v54, s3, -v151
	v_exp_f32_e32 v157, v36
	v_fma_f32 v36, v38, s3, -v151
	v_fma_f32 v38, v55, s3, -v151
	v_exp_f32_e32 v158, v36
	v_exp_f32_e32 v159, v38
	v_fma_f32 v38, v39, s3, -v151
	v_exp_f32_e32 v160, v38
	v_add_f32_e32 v52, v153, v154
	v_add_f32_e32 v36, 0, v52
	v_add_f32_e32 v37, v155, v156
	v_add_f32_e32 v36, v37, v36
	v_add_f32_e32 v37, v157, v158
	v_fma_f32 v38, v56, s3, -v151
	v_add_f32_e32 v36, v37, v36
	v_add_f32_e32 v37, v159, v160
	v_exp_f32_e32 v161, v38
	v_fma_f32 v38, v40, s3, -v151
	v_add_f32_e32 v40, v37, v36
	v_fma_f32 v36, v57, s3, -v151
	v_exp_f32_e32 v163, v36
	v_fma_f32 v36, v41, s3, -v151
	v_exp_f32_e32 v164, v36
	v_fma_f32 v36, v58, s3, -v151
	v_exp_f32_e32 v162, v38
	v_exp_f32_e32 v37, v36
	v_fma_f32 v36, v42, s3, -v151
	v_exp_f32_e32 v39, v36
	v_fma_f32 v36, v59, s3, -v151
	v_fma_f32 v38, v43, s3, -v151
	v_exp_f32_e32 v36, v36
	v_exp_f32_e32 v38, v38
	v_add_f32_e32 v52, v161, v162
	v_add_f32_e32 v40, v52, v40
	v_add_f32_e32 v41, v163, v164
	v_add_f32_e32 v42, v41, v40
	v_pk_add_f32 v[40:41], v[36:37], v[38:39]
	v_add_f32_e32 v41, v41, v42
	v_fma_f32 v42, v60, s3, -v151
	v_exp_f32_e32 v43, v42
	v_fma_f32 v42, v44, s3, -v151
	v_exp_f32_e32 v53, v42
	v_fma_f32 v42, v61, s3, -v151
	v_fma_f32 v44, v45, s3, -v151
	v_exp_f32_e32 v42, v42
	v_exp_f32_e32 v52, v44
	v_add_f32_e32 v44, v40, v41
	s_andn2_b64 vcc, exec, s[18:19]
	v_pk_add_f32 v[40:41], v[42:43], v[52:53]
	v_pk_mov_b32 v[56:57], v[52:53], v[52:53] op_sel:[1,0]
	v_add_f32_e32 v41, v41, v44
	v_fma_f32 v44, v62, s3, -v151
	v_exp_f32_e32 v45, v44
	v_fma_f32 v44, v46, s3, -v151
	v_exp_f32_e32 v55, v44
	v_fma_f32 v44, v63, s3, -v151
	v_fma_f32 v46, v47, s3, -v151
	v_exp_f32_e32 v44, v44
	v_exp_f32_e32 v54, v46
	v_add_f32_e32 v46, v40, v41
	v_pk_mov_b32 v[58:59], v[44:45], v[44:45] op_sel:[1,0]
	v_pk_add_f32 v[40:41], v[44:45], v[54:55]
	v_pk_mov_b32 v[54:55], v[54:55], v[54:55] op_sel:[1,0]
	v_add_f32_e32 v41, v41, v46
	v_fma_f32 v46, v64, s3, -v151
	v_exp_f32_e32 v47, v46
	v_fma_f32 v46, v48, s3, -v151
	v_exp_f32_e32 v53, v46
	v_fma_f32 v46, v65, s3, -v151
	v_fma_f32 v48, v49, s3, -v151
	v_exp_f32_e32 v46, v46
	v_exp_f32_e32 v52, v48
	v_add_f32_e32 v44, v40, v41
	v_fma_f32 v48, v51, s3, -v151
	v_exp_f32_e32 v48, v48
	v_pk_add_f32 v[40:41], v[46:47], v[52:53]
	v_pk_mov_b32 v[60:61], v[52:53], v[52:53] op_sel:[1,0]
	v_add_f32_e32 v41, v41, v44
	v_fma_f32 v44, v66, s3, -v151
	v_exp_f32_e32 v45, v44
	v_fma_f32 v44, v50, s3, -v151
	v_exp_f32_e32 v49, v44
	v_fma_f32 v44, v67, s3, -v151
	v_exp_f32_e32 v44, v44
	v_add_f32_e32 v50, v40, v41
	v_pk_mov_b32 v[64:65], v[48:49], v[48:49] op_sel:[1,0]
	v_pk_add_f32 v[40:41], v[44:45], v[48:49]
	v_pk_mov_b32 v[62:63], v[44:45], v[44:45] op_sel:[1,0]
	v_add_f32_e32 v41, v41, v50
	v_add_f32_e32 v52, v40, v41
	ds_bpermute_b32 v53, v152, v52
	v_cvt_pk_bf16_f32 v48, v153, v155
	v_cvt_pk_bf16_f32 v49, v157, v159
	v_cvt_pk_bf16_f32 v50, v161, v163
	v_cvt_pk_bf16_f32 v51, v37, v36
	v_cvt_pk_bf16_f32 v44, v43, v42
	v_cvt_pk_bf16_f32 v45, v58, v59
	v_cvt_pk_bf16_f32 v46, v47, v46
	v_cvt_pk_bf16_f32 v47, v62, v63
	v_cvt_pk_bf16_f32 v40, v154, v156
	v_cvt_pk_bf16_f32 v41, v158, v160
	v_cvt_pk_bf16_f32 v42, v162, v164
	v_cvt_pk_bf16_f32 v43, v39, v38
	v_cvt_pk_bf16_f32 v36, v56, v57
	v_cvt_pk_bf16_f32 v37, v54, v55
	v_cvt_pk_bf16_f32 v38, v60, v61
	v_cvt_pk_bf16_f32 v39, v64, v65
	s_mov_b64 s[12:13], -1
	s_cbranch_vccnz .LBB0_832
	v_add3_u32 v58, s4, v146, v125
	v_add_u32_e32 v59, 0x3000, v58
	ds_read2_b64 v[54:57], v59 offset0:128 offset1:130
	v_add_u32_e32 v58, 0x4000, v58
	s_mov_b64 s[12:13], 0
	s_waitcnt lgkmcnt(0)
	v_mfma_f32_32x32x16_bf16 v[20:35], v[54:57], v[48:51], v[20:35]
	ds_read2_b64 v[54:57], v58 offset0:160 offset1:162
	s_waitcnt lgkmcnt(0)
	v_mfma_f32_32x32x16_bf16 v[4:19], v[54:57], v[48:51], v[4:19]
	ds_read2_b64 v[54:57], v59 offset0:132 offset1:134
	s_waitcnt lgkmcnt(0)
	v_mfma_f32_32x32x16_bf16 v[20:35], v[54:57], v[44:47], v[20:35]
	ds_read2_b64 v[54:57], v58 offset0:164 offset1:166
	s_waitcnt lgkmcnt(0)
	v_mfma_f32_32x32x16_bf16 v[4:19], v[54:57], v[44:47], v[4:19]
	ds_read2_b64 v[54:57], v59 offset0:136 offset1:138
	s_waitcnt lgkmcnt(0)
	v_mfma_f32_32x32x16_bf16 v[20:35], v[54:57], v[40:43], v[20:35]
	ds_read2_b64 v[54:57], v58 offset0:168 offset1:170
	s_waitcnt lgkmcnt(0)
	v_mfma_f32_32x32x16_bf16 v[4:19], v[54:57], v[40:43], v[4:19]
	ds_read2_b64 v[54:57], v59 offset0:140 offset1:142
	s_waitcnt lgkmcnt(0)
	v_mfma_f32_32x32x16_bf16 v[20:35], v[54:57], v[36:39], v[20:35]
	ds_read2_b64 v[54:57], v58 offset0:172 offset1:174
	s_waitcnt lgkmcnt(0)
	v_mfma_f32_32x32x16_bf16 v[4:19], v[54:57], v[36:39], v[4:19]
	s_branch .LBB0_833

.LBB0_845:
	v_mul_f32_e32 v2, 0x3e16c740, v69
	v_fma_f32 v36, v36, s3, -v2
	v_exp_f32_e32 v70, v36
	v_fma_f32 v36, v53, s3, -v2
	v_fma_f32 v52, v52, s3, -v2
	v_exp_f32_e32 v71, v36
	v_fma_f32 v36, v37, s3, -v2
	v_exp_f32_e32 v69, v52
	v_exp_f32_e32 v72, v36
	v_fma_f32 v36, v54, s3, -v2
	v_exp_f32_e32 v73, v36
	v_fma_f32 v36, v38, s3, -v2
	v_fma_f32 v38, v55, s3, -v2
	v_exp_f32_e32 v74, v36
	v_exp_f32_e32 v75, v38
	v_fma_f32 v38, v39, s3, -v2
	v_exp_f32_e32 v76, v38
	v_add_f32_e32 v52, v69, v70
	v_add_f32_e32 v36, 0, v52
	v_add_f32_e32 v37, v71, v72
	v_add_f32_e32 v36, v37, v36
	v_add_f32_e32 v37, v73, v74
	v_fma_f32 v38, v56, s3, -v2
	v_add_f32_e32 v36, v37, v36
	v_add_f32_e32 v37, v75, v76
	v_exp_f32_e32 v77, v38
	v_fma_f32 v38, v40, s3, -v2
	v_add_f32_e32 v40, v37, v36
	v_fma_f32 v36, v57, s3, -v2
	v_exp_f32_e32 v79, v36
	v_fma_f32 v36, v41, s3, -v2
	v_exp_f32_e32 v80, v36
	v_fma_f32 v36, v58, s3, -v2
	v_exp_f32_e32 v78, v38
	v_exp_f32_e32 v37, v36
	v_fma_f32 v36, v42, s3, -v2
	v_exp_f32_e32 v39, v36
	v_fma_f32 v36, v59, s3, -v2
	v_fma_f32 v38, v43, s3, -v2
	v_exp_f32_e32 v36, v36
	v_exp_f32_e32 v38, v38
	v_add_f32_e32 v52, v77, v78
	v_add_f32_e32 v40, v52, v40
	v_add_f32_e32 v41, v79, v80
	v_add_f32_e32 v42, v41, v40
	v_pk_add_f32 v[40:41], v[36:37], v[38:39]
	v_add_f32_e32 v41, v41, v42
	v_fma_f32 v42, v60, s3, -v2
	v_exp_f32_e32 v43, v42
	v_fma_f32 v42, v44, s3, -v2
	v_exp_f32_e32 v53, v42
	v_fma_f32 v42, v61, s3, -v2
	v_fma_f32 v44, v45, s3, -v2
	v_exp_f32_e32 v42, v42
	v_exp_f32_e32 v52, v44
	v_add_f32_e32 v44, v40, v41
	s_andn2_b64 vcc, exec, s[18:19]
	v_pk_add_f32 v[40:41], v[42:43], v[52:53]
	v_pk_mov_b32 v[56:57], v[52:53], v[52:53] op_sel:[1,0]
	v_add_f32_e32 v41, v41, v44
	v_fma_f32 v44, v62, s3, -v2
	v_exp_f32_e32 v45, v44
	v_fma_f32 v44, v46, s3, -v2
	v_exp_f32_e32 v55, v44
	v_fma_f32 v44, v63, s3, -v2
	v_fma_f32 v46, v47, s3, -v2
	v_exp_f32_e32 v44, v44
	v_exp_f32_e32 v54, v46
	v_add_f32_e32 v46, v40, v41
	v_pk_mov_b32 v[58:59], v[44:45], v[44:45] op_sel:[1,0]
	v_pk_add_f32 v[40:41], v[44:45], v[54:55]
	v_pk_mov_b32 v[54:55], v[54:55], v[54:55] op_sel:[1,0]
	v_add_f32_e32 v41, v41, v46
	v_fma_f32 v46, v64, s3, -v2
	v_exp_f32_e32 v47, v46
	v_fma_f32 v46, v48, s3, -v2
	v_exp_f32_e32 v53, v46
	v_fma_f32 v46, v65, s3, -v2
	v_fma_f32 v48, v49, s3, -v2
	v_exp_f32_e32 v46, v46
	v_exp_f32_e32 v52, v48
	v_add_f32_e32 v44, v40, v41
	s_mov_b64 s[4:5], -1
	v_pk_add_f32 v[40:41], v[46:47], v[52:53]
	s_nop 0
	v_add_f32_e32 v41, v41, v44
	v_fma_f32 v44, v66, s3, -v2
	v_exp_f32_e32 v45, v44
	v_fma_f32 v44, v50, s3, -v2
	v_exp_f32_e32 v49, v44
	v_fma_f32 v44, v67, s3, -v2
	v_fma_f32 v2, v51, s3, -v2
	v_exp_f32_e32 v44, v44
	v_exp_f32_e32 v48, v2
	v_add_f32_e32 v2, v40, v41
	v_pk_mov_b32 v[60:61], v[52:53], v[52:53] op_sel:[1,0]
	v_pk_add_f32 v[40:41], v[44:45], v[48:49]
	v_pk_mov_b32 v[62:63], v[44:45], v[44:45] op_sel:[1,0]
	v_add_f32_e32 v2, v41, v2
	v_add_f32_e32 v2, v40, v2
	ds_bpermute_b32 v52, v68, v2
	v_pk_mov_b32 v[64:65], v[48:49], v[48:49] op_sel:[1,0]
	v_cvt_pk_bf16_f32 v48, v69, v71
	v_cvt_pk_bf16_f32 v49, v73, v75
	v_cvt_pk_bf16_f32 v50, v77, v79
	v_cvt_pk_bf16_f32 v51, v37, v36
	v_cvt_pk_bf16_f32 v44, v43, v42
	v_cvt_pk_bf16_f32 v45, v58, v59
	v_cvt_pk_bf16_f32 v46, v47, v46
	v_cvt_pk_bf16_f32 v47, v62, v63
	v_cvt_pk_bf16_f32 v40, v70, v72
	v_cvt_pk_bf16_f32 v41, v74, v76
	v_cvt_pk_bf16_f32 v42, v78, v80
	v_cvt_pk_bf16_f32 v43, v39, v38
	v_cvt_pk_bf16_f32 v36, v56, v57
	v_cvt_pk_bf16_f32 v37, v54, v55
	v_cvt_pk_bf16_f32 v38, v60, v61
	v_cvt_pk_bf16_f32 v39, v64, v65
	s_cbranch_vccnz .LBB0_847
	v_add3_u32 v53, s42, v146, v125
	v_add_u32_e32 v58, 0x3000, v53
	ds_read2_b64 v[54:57], v58 offset0:128 offset1:130
	v_add_u32_e32 v53, 0x4000, v53
	s_mov_b64 s[4:5], 0
	s_waitcnt lgkmcnt(0)
	v_mfma_f32_32x32x16_bf16 v[20:35], v[54:57], v[48:51], v[20:35]
	ds_read2_b64 v[54:57], v53 offset0:160 offset1:162
	s_waitcnt lgkmcnt(0)
	v_mfma_f32_32x32x16_bf16 v[4:19], v[54:57], v[48:51], v[4:19]
	ds_read2_b64 v[54:57], v58 offset0:132 offset1:134
	s_waitcnt lgkmcnt(0)
	v_mfma_f32_32x32x16_bf16 v[20:35], v[54:57], v[44:47], v[20:35]
	ds_read2_b64 v[54:57], v53 offset0:164 offset1:166
	s_waitcnt lgkmcnt(0)
	v_mfma_f32_32x32x16_bf16 v[4:19], v[54:57], v[44:47], v[4:19]
	ds_read2_b64 v[54:57], v58 offset0:136 offset1:138
	s_waitcnt lgkmcnt(0)
	v_mfma_f32_32x32x16_bf16 v[20:35], v[54:57], v[40:43], v[20:35]
	ds_read2_b64 v[54:57], v53 offset0:168 offset1:170
	s_waitcnt lgkmcnt(0)
	v_mfma_f32_32x32x16_bf16 v[4:19], v[54:57], v[40:43], v[4:19]
	ds_read2_b64 v[54:57], v58 offset0:140 offset1:142
	s_waitcnt lgkmcnt(0)
	v_mfma_f32_32x32x16_bf16 v[20:35], v[54:57], v[36:39], v[20:35]
	ds_read2_b64 v[54:57], v53 offset0:172 offset1:174
	s_waitcnt lgkmcnt(0)
	v_mfma_f32_32x32x16_bf16 v[4:19], v[54:57], v[36:39], v[4:19]
	s_branch .LBB0_848
